# alternating s_setprio between wave halves every half tile
# baseline (speedup 1.0000x reference)
.Lattn_pb0_0:
	s_waitcnt lgkmcnt(6)
	v_mfma_f32_16x16x32_bf16 v[64:67], v[160:163], v[96:99], 0
	v_exp_f32_e32 v88, v88
	v_mfma_f32_16x16x32_bf16 v[68:71], v[160:163], v[112:115], 0
	v_exp_f32_e32 v92, v92
	ds_read_b128 v[234:237], v209 offset:6144
	s_add_u32 s16, s22, s10
	s_addc_u32 s17, s23, s11
	s_add_u32 s15, s22, s12
	s_addc_u32 s14, s23, s13
	s_add_u32 s8, s16, 0x3bc00200
	s_addc_u32 s9, s17, 0
	s_add_u32 s6, s15, 0x23a50000
	s_addc_u32 s7, s14, 0
	s_waitcnt lgkmcnt(6)
	v_mfma_f32_16x16x32_bf16 v[0:3], v[164:167], v[216:219], v[0:3]
	v_cvt_pk_bf16_f32 v242, v80, v81
	v_mfma_f32_16x16x32_bf16 v[4:7], v[164:167], v[238:241], v[4:7]
	v_exp_f32_e32 v89, v89
	ds_read_b128 v[160:163], v201 offset:20480
	s_waitcnt vmcnt(4)
	ds_write_b128 v225, v[152:155] offset:49152
	s_waitcnt lgkmcnt(7)
	v_mfma_f32_16x16x32_bf16 v[68:71], v[168:171], v[116:119], v[68:71]
	v_exp_f32_e32 v93, v93
	v_mfma_f32_16x16x32_bf16 v[64:67], v[168:171], v[100:103], v[64:67]
	v_cvt_pk_bf16_f32 v243, v82, v83
	ds_read_b128 v[164:167], v209 offset:8192
	ds_write_b128 v226, v[156:159] offset:49152
	s_waitcnt lgkmcnt(8)
	v_mfma_f32_16x16x32_bf16 v[12:15], v[172:175], v[238:241], v[12:15]
	v_exp_f32_e32 v90, v90
	v_mfma_f32_16x16x32_bf16 v[8:11], v[172:175], v[216:219], v[8:11]
	v_exp_f32_e32 v94, v94
	ds_read_b128 v[168:171], v202 offset:20480
	ds_write_b64 v227, v[132:133] offset:32768
	s_waitcnt lgkmcnt(9)
	v_mfma_f32_16x16x32_bf16 v[64:67], v[176:179], v[104:107], v[64:67]
	v_cvt_pk_bf16_f32 v204, v84, v85
	v_mfma_f32_16x16x32_bf16 v[68:71], v[176:179], v[120:123], v[68:71]
	v_exp_f32_e32 v91, v91
	ds_read_b128 v[172:175], v209 offset:10240
	ds_write_b64 v228, v[134:135] offset:32768
	s_waitcnt lgkmcnt(10)
	v_mfma_f32_16x16x32_bf16 v[16:19], v[180:183], v[216:219], v[16:19]
	v_exp_f32_e32 v95, v95
	v_mfma_f32_16x16x32_bf16 v[20:23], v[180:183], v[238:241], v[20:23]
	v_cvt_pk_bf16_f32 v205, v86, v87
	v_add_f32_e32 v220, v220, v88
	ds_read_b128 v[176:179], v203 offset:20480
	ds_write_b64 v229, v[128:129] offset:32768
	s_waitcnt lgkmcnt(11)
	v_mfma_f32_16x16x32_bf16 v[68:71], v[230:233], v[124:127], v[68:71]
	v_add_f32_e32 v221, v221, v92
	v_add_f32_e32 v220, v220, v89
	v_mfma_f32_16x16x32_bf16 v[64:67], v[230:233], v[108:111], v[64:67]
	v_add_f32_e32 v221, v221, v93
	v_cvt_pk_bf16_f32 v244, v88, v89
	ds_read_b128 v[180:183], v209 offset:12288
	ds_write_b64 v184, v[130:131] offset:32768
	s_waitcnt lgkmcnt(12)
	v_mfma_f32_16x16x32_bf16 v[28:31], v[234:237], v[238:241], v[28:31]
	v_cvt_pk_bf16_f32 v245, v90, v91
	v_cvt_pk_bf16_f32 v206, v92, v93
	v_mfma_f32_16x16x32_bf16 v[24:27], v[234:237], v[216:219], v[24:27]
	v_cvt_pk_bf16_f32 v207, v94, v95
	ds_read_b128 v[230:233], v246 offset:20480
	global_load_dwordx4 v[132:135], v198, s[8:9]
	s_waitcnt lgkmcnt(12)
	v_mfma_f32_16x16x32_bf16 v[72:75], v[160:163], v[96:99], 0
	v_add_f32_e32 v220, v220, v90
	v_add_f32_e32 v221, v221, v94
	v_mfma_f32_16x16x32_bf16 v[76:79], v[160:163], v[112:115], 0
	v_add_f32_e32 v220, v220, v91
	v_add_f32_e32 v221, v221, v95
	ds_read_b128 v[234:237], v209 offset:14336
	global_load_dwordx4 v[128:131], v199, s[8:9]
	s_waitcnt lgkmcnt(11)
	v_mfma_f32_16x16x32_bf16 v[32:35], v[164:167], v[216:219], v[32:35]
	v_add_f32_e32 v194, v194, v220
	v_add_f32_e32 v195, v195, v221
	v_mfma_f32_16x16x32_bf16 v[36:39], v[164:167], v[238:241], v[36:39]
	v_exp_f32_e32 v64, v64
	ds_read_b128 v[160:163], v201 offset:24576
	global_load_dwordx4 v[152:155], v196, s[6:7]
	s_waitcnt lgkmcnt(10)
	v_mfma_f32_16x16x32_bf16 v[76:79], v[168:171], v[116:119], v[76:79]
	v_exp_f32_e32 v68, v68
	v_mfma_f32_16x16x32_bf16 v[72:75], v[168:171], v[100:103], v[72:75]
	v_exp_f32_e32 v65, v65
	ds_read_b128 v[164:167], v210 offset:0
	global_load_dwordx4 v[156:159], v197, s[6:7]
	s_waitcnt lgkmcnt(9)
	v_mfma_f32_16x16x32_bf16 v[44:47], v[172:175], v[238:241], v[44:47]
	v_exp_f32_e32 v69, v69
	v_mfma_f32_16x16x32_bf16 v[40:43], v[172:175], v[216:219], v[40:43]
	v_exp_f32_e32 v66, v66
	ds_read_b128 v[168:171], v202 offset:24576
	s_waitcnt lgkmcnt(8)
	v_mfma_f32_16x16x32_bf16 v[72:75], v[176:179], v[104:107], v[72:75]
	v_exp_f32_e32 v70, v70
	v_mfma_f32_16x16x32_bf16 v[76:79], v[176:179], v[120:123], v[76:79]
	v_exp_f32_e32 v67, v67
	ds_read_b128 v[172:175], v210 offset:2048
	s_waitcnt lgkmcnt(7)
	v_mfma_f32_16x16x32_bf16 v[48:51], v[180:183], v[216:219], v[48:51]
	v_exp_f32_e32 v71, v71
	v_mfma_f32_16x16x32_bf16 v[52:55], v[180:183], v[238:241], v[52:55]
	v_add_f32_e32 v220, v64, v65
	ds_read_b128 v[176:179], v203 offset:24576
	s_waitcnt lgkmcnt(6)
	v_mfma_f32_16x16x32_bf16 v[76:79], v[230:233], v[124:127], v[76:79]
	v_add_f32_e32 v221, v68, v69
	v_mfma_f32_16x16x32_bf16 v[72:75], v[230:233], v[108:111], v[72:75]
	v_add_f32_e32 v220, v220, v66
	ds_read_b128 v[180:183], v210 offset:4096
	s_waitcnt lgkmcnt(6)
	v_mfma_f32_16x16x32_bf16 v[60:63], v[234:237], v[238:241], v[60:63]
	v_add_f32_e32 v221, v221, v70
	v_add_f32_e32 v220, v220, v67
	v_mfma_f32_16x16x32_bf16 v[56:59], v[234:237], v[216:219], v[56:59]
	v_add_f32_e32 v221, v221, v71
	ds_read_b128 v[230:233], v246 offset:24576
	s_cmp_eq_u32 s100, 1
	s_cbranch_scc1 .Lattn_pa0_16
	s_setprio 1
	s_branch .Lattn_pb0_16

.Lattn_pb0_16:
	s_waitcnt lgkmcnt(6)
	v_mfma_f32_16x16x32_bf16 v[80:83], v[160:163], v[96:99], 0
	v_exp_f32_e32 v72, v72
	v_mfma_f32_16x16x32_bf16 v[84:87], v[160:163], v[112:115], 0
	v_exp_f32_e32 v76, v76
	ds_read_b128 v[234:237], v210 offset:6144
	s_waitcnt lgkmcnt(6)
	v_mfma_f32_16x16x32_bf16 v[0:3], v[164:167], v[242:245], v[0:3]
	v_exp_f32_e32 v73, v73
	v_mfma_f32_16x16x32_bf16 v[4:7], v[164:167], v[204:207], v[4:7]
	v_exp_f32_e32 v77, v77
	ds_read_b128 v[160:163], v201 offset:28672
	s_waitcnt lgkmcnt(6)
	v_mfma_f32_16x16x32_bf16 v[84:87], v[168:171], v[116:119], v[84:87]
	v_exp_f32_e32 v74, v74
	v_mfma_f32_16x16x32_bf16 v[80:83], v[168:171], v[100:103], v[80:83]
	v_exp_f32_e32 v78, v78
	ds_read_b128 v[164:167], v210 offset:8192
	s_waitcnt lgkmcnt(6)
	v_mfma_f32_16x16x32_bf16 v[12:15], v[172:175], v[204:207], v[12:15]
	v_exp_f32_e32 v75, v75
	v_mfma_f32_16x16x32_bf16 v[8:11], v[172:175], v[242:245], v[8:11]
	v_exp_f32_e32 v79, v79
	ds_read_b128 v[168:171], v202 offset:28672
	s_waitcnt lgkmcnt(6)
	v_mfma_f32_16x16x32_bf16 v[80:83], v[176:179], v[104:107], v[80:83]
	v_add_f32_e32 v220, v220, v72
	v_add_f32_e32 v221, v221, v76
	v_mfma_f32_16x16x32_bf16 v[84:87], v[176:179], v[120:123], v[84:87]
	v_add_f32_e32 v220, v220, v73
	ds_read_b128 v[172:175], v210 offset:10240
	s_waitcnt lgkmcnt(6)
	v_mfma_f32_16x16x32_bf16 v[16:19], v[180:183], v[242:245], v[16:19]
	v_add_f32_e32 v221, v221, v77
	v_add_f32_e32 v220, v220, v74
	v_mfma_f32_16x16x32_bf16 v[20:23], v[180:183], v[204:207], v[20:23]
	v_add_f32_e32 v221, v221, v78
	ds_read_b128 v[176:179], v203 offset:28672
	s_waitcnt lgkmcnt(6)
	v_mfma_f32_16x16x32_bf16 v[84:87], v[230:233], v[124:127], v[84:87]
	v_add_f32_e32 v220, v220, v75
	v_add_f32_e32 v221, v221, v79
	v_mfma_f32_16x16x32_bf16 v[80:83], v[230:233], v[108:111], v[80:83]
	v_cvt_pk_bf16_f32 v216, v64, v65
	ds_read_b128 v[180:183], v210 offset:12288
	s_waitcnt lgkmcnt(6)
	v_mfma_f32_16x16x32_bf16 v[28:31], v[234:237], v[204:207], v[28:31]
	v_cvt_pk_bf16_f32 v217, v66, v67
	v_cvt_pk_bf16_f32 v238, v68, v69
	v_mfma_f32_16x16x32_bf16 v[24:27], v[234:237], v[242:245], v[24:27]
	v_cvt_pk_bf16_f32 v239, v70, v71
	ds_read_b128 v[230:233], v246 offset:28672
	s_waitcnt lgkmcnt(6)
	v_mfma_f32_16x16x32_bf16 v[88:91], v[160:163], v[96:99], 0
	v_exp_f32_e32 v80, v80
	v_mfma_f32_16x16x32_bf16 v[92:95], v[160:163], v[112:115], 0
	v_exp_f32_e32 v84, v84
	ds_read_b128 v[234:237], v210 offset:14336
	s_waitcnt lgkmcnt(6)
	v_mfma_f32_16x16x32_bf16 v[32:35], v[164:167], v[242:245], v[32:35]
	v_exp_f32_e32 v81, v81
	v_mfma_f32_16x16x32_bf16 v[36:39], v[164:167], v[204:207], v[36:39]
	v_exp_f32_e32 v85, v85
	ds_read_b128 v[160:163], v201 offset:32768
	s_waitcnt lgkmcnt(6)
	v_mfma_f32_16x16x32_bf16 v[92:95], v[168:171], v[116:119], v[92:95]
	v_exp_f32_e32 v82, v82
	v_mfma_f32_16x16x32_bf16 v[88:91], v[168:171], v[100:103], v[88:91]
	v_exp_f32_e32 v86, v86
	ds_read_b128 v[164:167], v209 offset:16384
	s_waitcnt lgkmcnt(6)
	v_mfma_f32_16x16x32_bf16 v[44:47], v[172:175], v[204:207], v[44:47]
	v_exp_f32_e32 v83, v83
	v_mfma_f32_16x16x32_bf16 v[40:43], v[172:175], v[242:245], v[40:43]
	v_exp_f32_e32 v87, v87
	ds_read_b128 v[168:171], v202 offset:32768
	s_waitcnt lgkmcnt(6)
	v_mfma_f32_16x16x32_bf16 v[88:91], v[176:179], v[104:107], v[88:91]
	v_add_f32_e32 v220, v220, v80
	v_add_f32_e32 v221, v221, v84
	v_mfma_f32_16x16x32_bf16 v[92:95], v[176:179], v[120:123], v[92:95]
	v_add_f32_e32 v220, v220, v81
	ds_read_b128 v[172:175], v209 offset:18432
	s_waitcnt lgkmcnt(6)
	v_mfma_f32_16x16x32_bf16 v[48:51], v[180:183], v[242:245], v[48:51]
	v_add_f32_e32 v221, v221, v85
	v_add_f32_e32 v220, v220, v82
	v_mfma_f32_16x16x32_bf16 v[52:55], v[180:183], v[204:207], v[52:55]
	v_add_f32_e32 v221, v221, v86
	ds_read_b128 v[176:179], v203 offset:32768
	s_waitcnt lgkmcnt(6)
	v_mfma_f32_16x16x32_bf16 v[92:95], v[230:233], v[124:127], v[92:95]
	v_add_f32_e32 v220, v220, v83
	v_add_f32_e32 v221, v221, v87
	v_mfma_f32_16x16x32_bf16 v[88:91], v[230:233], v[108:111], v[88:91]
	v_cvt_pk_bf16_f32 v218, v72, v73
	ds_read_b128 v[180:183], v209 offset:20480
	s_waitcnt lgkmcnt(6)
	v_mfma_f32_16x16x32_bf16 v[60:63], v[234:237], v[204:207], v[60:63]
	v_cvt_pk_bf16_f32 v219, v74, v75
	v_cvt_pk_bf16_f32 v240, v76, v77
	v_mfma_f32_16x16x32_bf16 v[56:59], v[234:237], v[242:245], v[56:59]
	v_cvt_pk_bf16_f32 v241, v78, v79
	ds_read_b128 v[230:233], v246 offset:32768
	s_cmp_eq_u32 s100, 0
	s_cbranch_scc1 .Lattn_pa1_0
	s_setprio 1
	s_branch .Lattn_pb1_0

.Lattn_pb1_0:
	s_waitcnt lgkmcnt(6)
	v_mfma_f32_16x16x32_bf16 v[64:67], v[160:163], v[96:99], 0
	v_exp_f32_e32 v88, v88
	v_mfma_f32_16x16x32_bf16 v[68:71], v[160:163], v[112:115], 0
	v_exp_f32_e32 v92, v92
	ds_read_b128 v[234:237], v209 offset:22528
	s_add_u32 s8, s16, 0x3bc00280
	s_addc_u32 s9, s17, 0
	s_add_u32 s6, s15, 0x23a60000
	s_addc_u32 s7, s14, 0
	s_waitcnt lgkmcnt(6)
	v_mfma_f32_16x16x32_bf16 v[0:3], v[164:167], v[216:219], v[0:3]
	v_cvt_pk_bf16_f32 v242, v80, v81
	v_mfma_f32_16x16x32_bf16 v[4:7], v[164:167], v[238:241], v[4:7]
	v_exp_f32_e32 v89, v89
	ds_read_b128 v[160:163], v201 offset:36864
	s_waitcnt vmcnt(4)
	ds_write_b128 v225, v[136:139] offset:0
	s_waitcnt lgkmcnt(7)
	v_mfma_f32_16x16x32_bf16 v[68:71], v[168:171], v[116:119], v[68:71]
	v_exp_f32_e32 v93, v93
	v_mfma_f32_16x16x32_bf16 v[64:67], v[168:171], v[100:103], v[64:67]
	v_cvt_pk_bf16_f32 v243, v82, v83
	ds_read_b128 v[164:167], v209 offset:24576
	ds_write_b128 v226, v[140:143] offset:0
	s_waitcnt lgkmcnt(8)
	v_mfma_f32_16x16x32_bf16 v[12:15], v[172:175], v[238:241], v[12:15]
	v_exp_f32_e32 v90, v90
	v_mfma_f32_16x16x32_bf16 v[8:11], v[172:175], v[216:219], v[8:11]
	v_exp_f32_e32 v94, v94
	ds_read_b128 v[168:171], v202 offset:36864
	ds_write_b64 v227, v[148:149] offset:49152
	s_waitcnt lgkmcnt(9)
	v_mfma_f32_16x16x32_bf16 v[64:67], v[176:179], v[104:107], v[64:67]
	v_cvt_pk_bf16_f32 v204, v84, v85
	v_mfma_f32_16x16x32_bf16 v[68:71], v[176:179], v[120:123], v[68:71]
	v_exp_f32_e32 v91, v91
	ds_read_b128 v[172:175], v209 offset:26624
	ds_write_b64 v228, v[150:151] offset:49152
	s_waitcnt lgkmcnt(10)
	v_mfma_f32_16x16x32_bf16 v[16:19], v[180:183], v[216:219], v[16:19]
	v_exp_f32_e32 v95, v95
	v_mfma_f32_16x16x32_bf16 v[20:23], v[180:183], v[238:241], v[20:23]
	v_cvt_pk_bf16_f32 v205, v86, v87
	v_add_f32_e32 v220, v220, v88
	ds_read_b128 v[176:179], v203 offset:36864
	ds_write_b64 v229, v[144:145] offset:49152
	s_waitcnt lgkmcnt(11)
	v_mfma_f32_16x16x32_bf16 v[68:71], v[230:233], v[124:127], v[68:71]
	v_add_f32_e32 v221, v221, v92
	v_add_f32_e32 v220, v220, v89
	v_mfma_f32_16x16x32_bf16 v[64:67], v[230:233], v[108:111], v[64:67]
	v_add_f32_e32 v221, v221, v93
	v_cvt_pk_bf16_f32 v244, v88, v89
	ds_read_b128 v[180:183], v209 offset:28672
	ds_write_b64 v184, v[146:147] offset:49152
	s_waitcnt lgkmcnt(12)
	v_mfma_f32_16x16x32_bf16 v[28:31], v[234:237], v[238:241], v[28:31]
	v_cvt_pk_bf16_f32 v245, v90, v91
	v_cvt_pk_bf16_f32 v206, v92, v93
	v_mfma_f32_16x16x32_bf16 v[24:27], v[234:237], v[216:219], v[24:27]
	v_cvt_pk_bf16_f32 v207, v94, v95
	ds_read_b128 v[230:233], v246 offset:36864
	global_load_dwordx4 v[148:151], v198, s[8:9]
	s_waitcnt lgkmcnt(12)
	v_mfma_f32_16x16x32_bf16 v[72:75], v[160:163], v[96:99], 0
	v_add_f32_e32 v220, v220, v90
	v_add_f32_e32 v221, v221, v94
	v_mfma_f32_16x16x32_bf16 v[76:79], v[160:163], v[112:115], 0
	v_add_f32_e32 v220, v220, v91
	v_add_f32_e32 v221, v221, v95
	ds_read_b128 v[234:237], v209 offset:30720
	global_load_dwordx4 v[144:147], v199, s[8:9]
	s_waitcnt lgkmcnt(11)
	v_mfma_f32_16x16x32_bf16 v[32:35], v[164:167], v[216:219], v[32:35]
	v_add_f32_e32 v194, v194, v220
	v_add_f32_e32 v195, v195, v221
	v_mfma_f32_16x16x32_bf16 v[36:39], v[164:167], v[238:241], v[36:39]
	v_exp_f32_e32 v64, v64
	ds_read_b128 v[160:163], v201 offset:40960
	global_load_dwordx4 v[136:139], v196, s[6:7]
	s_waitcnt lgkmcnt(10)
	v_mfma_f32_16x16x32_bf16 v[76:79], v[168:171], v[116:119], v[76:79]
	v_exp_f32_e32 v68, v68
	v_mfma_f32_16x16x32_bf16 v[72:75], v[168:171], v[100:103], v[72:75]
	v_exp_f32_e32 v65, v65
	ds_read_b128 v[164:167], v210 offset:16384
	global_load_dwordx4 v[140:143], v197, s[6:7]
	s_waitcnt lgkmcnt(9)
	v_mfma_f32_16x16x32_bf16 v[44:47], v[172:175], v[238:241], v[44:47]
	v_exp_f32_e32 v69, v69
	v_mfma_f32_16x16x32_bf16 v[40:43], v[172:175], v[216:219], v[40:43]
	v_exp_f32_e32 v66, v66
	ds_read_b128 v[168:171], v202 offset:40960
	s_waitcnt lgkmcnt(8)
	v_mfma_f32_16x16x32_bf16 v[72:75], v[176:179], v[104:107], v[72:75]
	v_exp_f32_e32 v70, v70
	v_mfma_f32_16x16x32_bf16 v[76:79], v[176:179], v[120:123], v[76:79]
	v_exp_f32_e32 v67, v67
	ds_read_b128 v[172:175], v210 offset:18432
	s_waitcnt lgkmcnt(7)
	v_mfma_f32_16x16x32_bf16 v[48:51], v[180:183], v[216:219], v[48:51]
	v_exp_f32_e32 v71, v71
	v_mfma_f32_16x16x32_bf16 v[52:55], v[180:183], v[238:241], v[52:55]
	v_add_f32_e32 v220, v64, v65
	ds_read_b128 v[176:179], v203 offset:40960
	s_waitcnt lgkmcnt(6)
	v_mfma_f32_16x16x32_bf16 v[76:79], v[230:233], v[124:127], v[76:79]
	v_add_f32_e32 v221, v68, v69
	v_mfma_f32_16x16x32_bf16 v[72:75], v[230:233], v[108:111], v[72:75]
	v_add_f32_e32 v220, v220, v66
	ds_read_b128 v[180:183], v210 offset:20480
	s_waitcnt lgkmcnt(6)
	v_mfma_f32_16x16x32_bf16 v[60:63], v[234:237], v[238:241], v[60:63]
	v_add_f32_e32 v221, v221, v70
	v_add_f32_e32 v220, v220, v67
	v_mfma_f32_16x16x32_bf16 v[56:59], v[234:237], v[216:219], v[56:59]
	v_add_f32_e32 v221, v221, v71
	ds_read_b128 v[230:233], v246 offset:40960
	s_cmp_eq_u32 s100, 1
	s_cbranch_scc1 .Lattn_pa1_16
	s_setprio 1
	s_branch .Lattn_pb1_16

.Lattn_pb1_16:
	s_waitcnt lgkmcnt(6)
	v_mfma_f32_16x16x32_bf16 v[80:83], v[160:163], v[96:99], 0
	v_exp_f32_e32 v72, v72
	v_mfma_f32_16x16x32_bf16 v[84:87], v[160:163], v[112:115], 0
	v_exp_f32_e32 v76, v76
	ds_read_b128 v[234:237], v210 offset:22528
	s_waitcnt lgkmcnt(6)
	v_mfma_f32_16x16x32_bf16 v[0:3], v[164:167], v[242:245], v[0:3]
	v_exp_f32_e32 v73, v73
	v_mfma_f32_16x16x32_bf16 v[4:7], v[164:167], v[204:207], v[4:7]
	v_exp_f32_e32 v77, v77
	ds_read_b128 v[160:163], v201 offset:45056
	s_waitcnt lgkmcnt(6)
	v_mfma_f32_16x16x32_bf16 v[84:87], v[168:171], v[116:119], v[84:87]
	v_exp_f32_e32 v74, v74
	v_mfma_f32_16x16x32_bf16 v[80:83], v[168:171], v[100:103], v[80:83]
	v_exp_f32_e32 v78, v78
	ds_read_b128 v[164:167], v210 offset:24576
	s_waitcnt lgkmcnt(6)
	v_mfma_f32_16x16x32_bf16 v[12:15], v[172:175], v[204:207], v[12:15]
	v_exp_f32_e32 v75, v75
	v_mfma_f32_16x16x32_bf16 v[8:11], v[172:175], v[242:245], v[8:11]
	v_exp_f32_e32 v79, v79
	ds_read_b128 v[168:171], v202 offset:45056
	s_waitcnt lgkmcnt(6)
	v_mfma_f32_16x16x32_bf16 v[80:83], v[176:179], v[104:107], v[80:83]
	v_add_f32_e32 v220, v220, v72
	v_add_f32_e32 v221, v221, v76
	v_mfma_f32_16x16x32_bf16 v[84:87], v[176:179], v[120:123], v[84:87]
	v_add_f32_e32 v220, v220, v73
	ds_read_b128 v[172:175], v210 offset:26624
	s_waitcnt lgkmcnt(6)
	v_mfma_f32_16x16x32_bf16 v[16:19], v[180:183], v[242:245], v[16:19]
	v_add_f32_e32 v221, v221, v77
	v_add_f32_e32 v220, v220, v74
	v_mfma_f32_16x16x32_bf16 v[20:23], v[180:183], v[204:207], v[20:23]
	v_add_f32_e32 v221, v221, v78
	ds_read_b128 v[176:179], v203 offset:45056
	s_waitcnt lgkmcnt(6)
	v_mfma_f32_16x16x32_bf16 v[84:87], v[230:233], v[124:127], v[84:87]
	v_add_f32_e32 v220, v220, v75
	v_add_f32_e32 v221, v221, v79
	v_mfma_f32_16x16x32_bf16 v[80:83], v[230:233], v[108:111], v[80:83]
	v_cvt_pk_bf16_f32 v216, v64, v65
	ds_read_b128 v[180:183], v210 offset:28672
	s_waitcnt lgkmcnt(6)
	v_mfma_f32_16x16x32_bf16 v[28:31], v[234:237], v[204:207], v[28:31]
	v_cvt_pk_bf16_f32 v217, v66, v67
	v_cvt_pk_bf16_f32 v238, v68, v69
	v_mfma_f32_16x16x32_bf16 v[24:27], v[234:237], v[242:245], v[24:27]
	v_cvt_pk_bf16_f32 v239, v70, v71
	ds_read_b128 v[230:233], v246 offset:45056
	s_waitcnt lgkmcnt(6)
	v_mfma_f32_16x16x32_bf16 v[88:91], v[160:163], v[96:99], 0
	v_exp_f32_e32 v80, v80
	v_mfma_f32_16x16x32_bf16 v[92:95], v[160:163], v[112:115], 0
	v_exp_f32_e32 v84, v84
	ds_read_b128 v[234:237], v210 offset:30720
	s_waitcnt lgkmcnt(6)
	v_mfma_f32_16x16x32_bf16 v[32:35], v[164:167], v[242:245], v[32:35]
	v_exp_f32_e32 v81, v81
	v_mfma_f32_16x16x32_bf16 v[36:39], v[164:167], v[204:207], v[36:39]
	v_exp_f32_e32 v85, v85
	s_waitcnt lgkmcnt(5)
	v_mfma_f32_16x16x32_bf16 v[92:95], v[168:171], v[116:119], v[92:95]
	v_exp_f32_e32 v82, v82
	v_mfma_f32_16x16x32_bf16 v[88:91], v[168:171], v[100:103], v[88:91]
	v_exp_f32_e32 v86, v86
	s_waitcnt lgkmcnt(4)
	v_mfma_f32_16x16x32_bf16 v[44:47], v[172:175], v[204:207], v[44:47]
	v_exp_f32_e32 v83, v83
	v_mfma_f32_16x16x32_bf16 v[40:43], v[172:175], v[242:245], v[40:43]
	v_exp_f32_e32 v87, v87
	s_waitcnt lgkmcnt(3)
	v_mfma_f32_16x16x32_bf16 v[88:91], v[176:179], v[104:107], v[88:91]
	v_add_f32_e32 v220, v220, v80
	v_add_f32_e32 v221, v221, v84
	v_mfma_f32_16x16x32_bf16 v[92:95], v[176:179], v[120:123], v[92:95]
	v_add_f32_e32 v220, v220, v81
	s_waitcnt lgkmcnt(2)
	v_mfma_f32_16x16x32_bf16 v[48:51], v[180:183], v[242:245], v[48:51]
	v_add_f32_e32 v221, v221, v85
	v_add_f32_e32 v220, v220, v82
	v_mfma_f32_16x16x32_bf16 v[52:55], v[180:183], v[204:207], v[52:55]
	v_add_f32_e32 v221, v221, v86
	s_waitcnt lgkmcnt(1)
	v_mfma_f32_16x16x32_bf16 v[92:95], v[230:233], v[124:127], v[92:95]
	v_add_f32_e32 v220, v220, v83
	v_add_f32_e32 v221, v221, v87
	v_mfma_f32_16x16x32_bf16 v[88:91], v[230:233], v[108:111], v[88:91]
	v_cvt_pk_bf16_f32 v218, v72, v73
	s_waitcnt lgkmcnt(0)
	v_mfma_f32_16x16x32_bf16 v[60:63], v[234:237], v[204:207], v[60:63]
	v_cvt_pk_bf16_f32 v219, v74, v75
	v_cvt_pk_bf16_f32 v240, v76, v77
	v_mfma_f32_16x16x32_bf16 v[56:59], v[234:237], v[242:245], v[56:59]
	v_cvt_pk_bf16_f32 v241, v78, v79
	s_waitcnt lgkmcnt(0)
	s_barrier
	ds_read_b128 v[160:163], v201 offset:49152
	ds_read_b128 v[164:167], v209 offset:32768
	ds_read_b128 v[168:171], v202 offset:49152
	ds_read_b128 v[172:175], v209 offset:34816
	ds_read_b128 v[176:179], v203 offset:49152
	ds_read_b128 v[180:183], v209 offset:36864
	ds_read_b128 v[230:233], v246 offset:49152
	s_cmp_eq_u32 s100, 0
	s_cbranch_scc1 .Lattn_pa2_0
	s_setprio 1
	s_branch .Lattn_pb2_0

.Lattn_pb2_0:
	s_waitcnt lgkmcnt(6)
	v_mfma_f32_16x16x32_bf16 v[64:67], v[160:163], v[96:99], 0
	v_exp_f32_e32 v88, v88
	v_mfma_f32_16x16x32_bf16 v[68:71], v[160:163], v[112:115], 0
	v_exp_f32_e32 v92, v92
	ds_read_b128 v[234:237], v209 offset:38912
	s_add_u32 s8, s16, 0x3bc00300
	s_addc_u32 s9, s17, 0
	s_add_u32 s6, s15, 0x23a70000
	s_addc_u32 s7, s14, 0
	s_waitcnt lgkmcnt(6)
	v_mfma_f32_16x16x32_bf16 v[0:3], v[164:167], v[216:219], v[0:3]
	v_cvt_pk_bf16_f32 v242, v80, v81
	v_mfma_f32_16x16x32_bf16 v[4:7], v[164:167], v[238:241], v[4:7]
	v_exp_f32_e32 v89, v89
	ds_read_b128 v[160:163], v201 offset:53248
	s_waitcnt vmcnt(4)
	ds_write_b128 v225, v[152:155] offset:16384
	s_waitcnt lgkmcnt(7)
	v_mfma_f32_16x16x32_bf16 v[68:71], v[168:171], v[116:119], v[68:71]
	v_exp_f32_e32 v93, v93
	v_mfma_f32_16x16x32_bf16 v[64:67], v[168:171], v[100:103], v[64:67]
	v_cvt_pk_bf16_f32 v243, v82, v83
	ds_read_b128 v[164:167], v209 offset:40960
	ds_write_b128 v226, v[156:159] offset:16384
	s_waitcnt lgkmcnt(8)
	v_mfma_f32_16x16x32_bf16 v[12:15], v[172:175], v[238:241], v[12:15]
	v_exp_f32_e32 v90, v90
	v_mfma_f32_16x16x32_bf16 v[8:11], v[172:175], v[216:219], v[8:11]
	v_exp_f32_e32 v94, v94
	ds_read_b128 v[168:171], v202 offset:53248
	ds_write_b64 v227, v[132:133] offset:0
	s_waitcnt lgkmcnt(9)
	v_mfma_f32_16x16x32_bf16 v[64:67], v[176:179], v[104:107], v[64:67]
	v_cvt_pk_bf16_f32 v204, v84, v85
	v_mfma_f32_16x16x32_bf16 v[68:71], v[176:179], v[120:123], v[68:71]
	v_exp_f32_e32 v91, v91
	ds_read_b128 v[172:175], v209 offset:43008
	ds_write_b64 v228, v[134:135] offset:0
	s_waitcnt lgkmcnt(10)
	v_mfma_f32_16x16x32_bf16 v[16:19], v[180:183], v[216:219], v[16:19]
	v_exp_f32_e32 v95, v95
	v_mfma_f32_16x16x32_bf16 v[20:23], v[180:183], v[238:241], v[20:23]
	v_cvt_pk_bf16_f32 v205, v86, v87
	v_add_f32_e32 v220, v220, v88
	ds_read_b128 v[176:179], v203 offset:53248
	ds_write_b64 v229, v[128:129] offset:0
	s_waitcnt lgkmcnt(11)
	v_mfma_f32_16x16x32_bf16 v[68:71], v[230:233], v[124:127], v[68:71]
	v_add_f32_e32 v221, v221, v92
	v_add_f32_e32 v220, v220, v89
	v_mfma_f32_16x16x32_bf16 v[64:67], v[230:233], v[108:111], v[64:67]
	v_add_f32_e32 v221, v221, v93
	v_cvt_pk_bf16_f32 v244, v88, v89
	ds_read_b128 v[180:183], v209 offset:45056
	ds_write_b64 v184, v[130:131] offset:0
	s_waitcnt lgkmcnt(12)
	v_mfma_f32_16x16x32_bf16 v[28:31], v[234:237], v[238:241], v[28:31]
	v_cvt_pk_bf16_f32 v245, v90, v91
	v_cvt_pk_bf16_f32 v206, v92, v93
	v_mfma_f32_16x16x32_bf16 v[24:27], v[234:237], v[216:219], v[24:27]
	v_cvt_pk_bf16_f32 v207, v94, v95
	ds_read_b128 v[230:233], v246 offset:53248
	global_load_dwordx4 v[132:135], v198, s[8:9]
	s_waitcnt lgkmcnt(12)
	v_mfma_f32_16x16x32_bf16 v[72:75], v[160:163], v[96:99], 0
	v_add_f32_e32 v220, v220, v90
	v_add_f32_e32 v221, v221, v94
	v_mfma_f32_16x16x32_bf16 v[76:79], v[160:163], v[112:115], 0
	v_add_f32_e32 v220, v220, v91
	v_add_f32_e32 v221, v221, v95
	ds_read_b128 v[234:237], v209 offset:47104
	global_load_dwordx4 v[128:131], v199, s[8:9]
	s_waitcnt lgkmcnt(11)
	v_mfma_f32_16x16x32_bf16 v[32:35], v[164:167], v[216:219], v[32:35]
	v_add_f32_e32 v194, v194, v220
	v_add_f32_e32 v195, v195, v221
	v_mfma_f32_16x16x32_bf16 v[36:39], v[164:167], v[238:241], v[36:39]
	v_exp_f32_e32 v64, v64
	ds_read_b128 v[160:163], v201 offset:57344
	global_load_dwordx4 v[152:155], v196, s[6:7]
	s_waitcnt lgkmcnt(10)
	v_mfma_f32_16x16x32_bf16 v[76:79], v[168:171], v[116:119], v[76:79]
	v_exp_f32_e32 v68, v68
	v_mfma_f32_16x16x32_bf16 v[72:75], v[168:171], v[100:103], v[72:75]
	v_exp_f32_e32 v65, v65
	ds_read_b128 v[164:167], v210 offset:32768
	global_load_dwordx4 v[156:159], v197, s[6:7]
	s_waitcnt lgkmcnt(9)
	v_mfma_f32_16x16x32_bf16 v[44:47], v[172:175], v[238:241], v[44:47]
	v_exp_f32_e32 v69, v69
	v_mfma_f32_16x16x32_bf16 v[40:43], v[172:175], v[216:219], v[40:43]
	v_exp_f32_e32 v66, v66
	ds_read_b128 v[168:171], v202 offset:57344
	s_waitcnt lgkmcnt(8)
	v_mfma_f32_16x16x32_bf16 v[72:75], v[176:179], v[104:107], v[72:75]
	v_exp_f32_e32 v70, v70
	v_mfma_f32_16x16x32_bf16 v[76:79], v[176:179], v[120:123], v[76:79]
	v_exp_f32_e32 v67, v67
	ds_read_b128 v[172:175], v210 offset:34816
	s_waitcnt lgkmcnt(7)
	v_mfma_f32_16x16x32_bf16 v[48:51], v[180:183], v[216:219], v[48:51]
	v_exp_f32_e32 v71, v71
	v_mfma_f32_16x16x32_bf16 v[52:55], v[180:183], v[238:241], v[52:55]
	v_add_f32_e32 v220, v64, v65
	ds_read_b128 v[176:179], v203 offset:57344
	s_waitcnt lgkmcnt(6)
	v_mfma_f32_16x16x32_bf16 v[76:79], v[230:233], v[124:127], v[76:79]
	v_add_f32_e32 v221, v68, v69
	v_mfma_f32_16x16x32_bf16 v[72:75], v[230:233], v[108:111], v[72:75]
	v_add_f32_e32 v220, v220, v66
	ds_read_b128 v[180:183], v210 offset:36864
	s_waitcnt lgkmcnt(6)
	v_mfma_f32_16x16x32_bf16 v[60:63], v[234:237], v[238:241], v[60:63]
	v_add_f32_e32 v221, v221, v70
	v_add_f32_e32 v220, v220, v67
	v_mfma_f32_16x16x32_bf16 v[56:59], v[234:237], v[216:219], v[56:59]
	v_add_f32_e32 v221, v221, v71
	ds_read_b128 v[230:233], v246 offset:57344
	s_cmp_eq_u32 s100, 1
	s_cbranch_scc1 .Lattn_pa2_16
	s_setprio 1
	s_branch .Lattn_pb2_16

.Lattn_pb2_16:
	s_waitcnt lgkmcnt(6)
	v_mfma_f32_16x16x32_bf16 v[80:83], v[160:163], v[96:99], 0
	v_exp_f32_e32 v72, v72
	v_mfma_f32_16x16x32_bf16 v[84:87], v[160:163], v[112:115], 0
	v_exp_f32_e32 v76, v76
	ds_read_b128 v[234:237], v210 offset:38912
	s_waitcnt lgkmcnt(6)
	v_mfma_f32_16x16x32_bf16 v[0:3], v[164:167], v[242:245], v[0:3]
	v_exp_f32_e32 v73, v73
	v_mfma_f32_16x16x32_bf16 v[4:7], v[164:167], v[204:207], v[4:7]
	v_exp_f32_e32 v77, v77
	ds_read_b128 v[160:163], v201 offset:61440
	s_waitcnt lgkmcnt(6)
	v_mfma_f32_16x16x32_bf16 v[84:87], v[168:171], v[116:119], v[84:87]
	v_exp_f32_e32 v74, v74
	v_mfma_f32_16x16x32_bf16 v[80:83], v[168:171], v[100:103], v[80:83]
	v_exp_f32_e32 v78, v78
	ds_read_b128 v[164:167], v210 offset:40960
	s_waitcnt lgkmcnt(6)
	v_mfma_f32_16x16x32_bf16 v[12:15], v[172:175], v[204:207], v[12:15]
	v_exp_f32_e32 v75, v75
	v_mfma_f32_16x16x32_bf16 v[8:11], v[172:175], v[242:245], v[8:11]
	v_exp_f32_e32 v79, v79
	ds_read_b128 v[168:171], v202 offset:61440
	s_waitcnt lgkmcnt(6)
	v_mfma_f32_16x16x32_bf16 v[80:83], v[176:179], v[104:107], v[80:83]
	v_add_f32_e32 v220, v220, v72
	v_add_f32_e32 v221, v221, v76
	v_mfma_f32_16x16x32_bf16 v[84:87], v[176:179], v[120:123], v[84:87]
	v_add_f32_e32 v220, v220, v73
	ds_read_b128 v[172:175], v210 offset:43008
	s_waitcnt lgkmcnt(6)
	v_mfma_f32_16x16x32_bf16 v[16:19], v[180:183], v[242:245], v[16:19]
	v_add_f32_e32 v221, v221, v77
	v_add_f32_e32 v220, v220, v74
	v_mfma_f32_16x16x32_bf16 v[20:23], v[180:183], v[204:207], v[20:23]
	v_add_f32_e32 v221, v221, v78
	ds_read_b128 v[176:179], v203 offset:61440
	s_waitcnt lgkmcnt(6)
	v_mfma_f32_16x16x32_bf16 v[84:87], v[230:233], v[124:127], v[84:87]
	v_add_f32_e32 v220, v220, v75
	v_add_f32_e32 v221, v221, v79
	v_mfma_f32_16x16x32_bf16 v[80:83], v[230:233], v[108:111], v[80:83]
	v_cvt_pk_bf16_f32 v216, v64, v65
	ds_read_b128 v[180:183], v210 offset:45056
	s_waitcnt lgkmcnt(6)
	v_mfma_f32_16x16x32_bf16 v[28:31], v[234:237], v[204:207], v[28:31]
	v_cvt_pk_bf16_f32 v217, v66, v67
	v_cvt_pk_bf16_f32 v238, v68, v69
	v_mfma_f32_16x16x32_bf16 v[24:27], v[234:237], v[242:245], v[24:27]
	v_cvt_pk_bf16_f32 v239, v70, v71
	ds_read_b128 v[230:233], v246 offset:61440
	s_waitcnt lgkmcnt(6)
	v_mfma_f32_16x16x32_bf16 v[88:91], v[160:163], v[96:99], 0
	v_exp_f32_e32 v80, v80
	v_mfma_f32_16x16x32_bf16 v[92:95], v[160:163], v[112:115], 0
	v_exp_f32_e32 v84, v84
	ds_read_b128 v[234:237], v210 offset:47104
	s_waitcnt lgkmcnt(6)
	v_mfma_f32_16x16x32_bf16 v[32:35], v[164:167], v[242:245], v[32:35]
	v_exp_f32_e32 v81, v81
	v_mfma_f32_16x16x32_bf16 v[36:39], v[164:167], v[204:207], v[36:39]
	v_exp_f32_e32 v85, v85
	ds_read_b128 v[160:163], v201 offset:0
	s_waitcnt lgkmcnt(6)
	v_mfma_f32_16x16x32_bf16 v[92:95], v[168:171], v[116:119], v[92:95]
	v_exp_f32_e32 v82, v82
	v_mfma_f32_16x16x32_bf16 v[88:91], v[168:171], v[100:103], v[88:91]
	v_exp_f32_e32 v86, v86
	ds_read_b128 v[164:167], v209 offset:49152
	s_waitcnt lgkmcnt(6)
	v_mfma_f32_16x16x32_bf16 v[44:47], v[172:175], v[204:207], v[44:47]
	v_exp_f32_e32 v83, v83
	v_mfma_f32_16x16x32_bf16 v[40:43], v[172:175], v[242:245], v[40:43]
	v_exp_f32_e32 v87, v87
	ds_read_b128 v[168:171], v202 offset:0
	s_waitcnt lgkmcnt(6)
	v_mfma_f32_16x16x32_bf16 v[88:91], v[176:179], v[104:107], v[88:91]
	v_add_f32_e32 v220, v220, v80
	v_add_f32_e32 v221, v221, v84
	v_mfma_f32_16x16x32_bf16 v[92:95], v[176:179], v[120:123], v[92:95]
	v_add_f32_e32 v220, v220, v81
	ds_read_b128 v[172:175], v209 offset:51200
	s_waitcnt lgkmcnt(6)
	v_mfma_f32_16x16x32_bf16 v[48:51], v[180:183], v[242:245], v[48:51]
	v_add_f32_e32 v221, v221, v85
	v_add_f32_e32 v220, v220, v82
	v_mfma_f32_16x16x32_bf16 v[52:55], v[180:183], v[204:207], v[52:55]
	v_add_f32_e32 v221, v221, v86
	ds_read_b128 v[176:179], v203 offset:0
	s_waitcnt lgkmcnt(6)
	v_mfma_f32_16x16x32_bf16 v[92:95], v[230:233], v[124:127], v[92:95]
	v_add_f32_e32 v220, v220, v83
	v_add_f32_e32 v221, v221, v87
	v_mfma_f32_16x16x32_bf16 v[88:91], v[230:233], v[108:111], v[88:91]
	v_cvt_pk_bf16_f32 v218, v72, v73
	ds_read_b128 v[180:183], v209 offset:53248
	s_waitcnt lgkmcnt(6)
	v_mfma_f32_16x16x32_bf16 v[60:63], v[234:237], v[204:207], v[60:63]
	v_cvt_pk_bf16_f32 v219, v74, v75
	v_cvt_pk_bf16_f32 v240, v76, v77
	v_mfma_f32_16x16x32_bf16 v[56:59], v[234:237], v[242:245], v[56:59]
	v_cvt_pk_bf16_f32 v241, v78, v79
	ds_read_b128 v[230:233], v246 offset:0
	s_cmp_eq_u32 s100, 0
	s_cbranch_scc1 .Lattn_pa3_0
	s_setprio 1
	s_branch .Lattn_pb3_0

.Lattn_pb3_0:
	s_waitcnt lgkmcnt(6)
	v_mfma_f32_16x16x32_bf16 v[64:67], v[160:163], v[96:99], 0
	v_exp_f32_e32 v88, v88
	v_mfma_f32_16x16x32_bf16 v[68:71], v[160:163], v[112:115], 0
	v_exp_f32_e32 v92, v92
	ds_read_b128 v[234:237], v209 offset:55296
	s_add_u32 s8, s16, 0x3bc00380
	s_addc_u32 s9, s17, 0
	s_add_u32 s6, s15, 0x23a80000
	s_addc_u32 s7, s14, 0
	s_waitcnt lgkmcnt(6)
	v_mfma_f32_16x16x32_bf16 v[0:3], v[164:167], v[216:219], v[0:3]
	v_cvt_pk_bf16_f32 v242, v80, v81
	v_mfma_f32_16x16x32_bf16 v[4:7], v[164:167], v[238:241], v[4:7]
	v_exp_f32_e32 v89, v89
	ds_read_b128 v[160:163], v201 offset:4096
	s_waitcnt vmcnt(4)
	ds_write_b128 v225, v[136:139] offset:32768
	s_waitcnt lgkmcnt(7)
	v_mfma_f32_16x16x32_bf16 v[68:71], v[168:171], v[116:119], v[68:71]
	v_exp_f32_e32 v93, v93
	v_mfma_f32_16x16x32_bf16 v[64:67], v[168:171], v[100:103], v[64:67]
	v_cvt_pk_bf16_f32 v243, v82, v83
	ds_read_b128 v[164:167], v209 offset:57344
	ds_write_b128 v226, v[140:143] offset:32768
	s_waitcnt lgkmcnt(8)
	v_mfma_f32_16x16x32_bf16 v[12:15], v[172:175], v[238:241], v[12:15]
	v_exp_f32_e32 v90, v90
	v_mfma_f32_16x16x32_bf16 v[8:11], v[172:175], v[216:219], v[8:11]
	v_exp_f32_e32 v94, v94
	ds_read_b128 v[168:171], v202 offset:4096
	ds_write_b64 v227, v[148:149] offset:16384
	s_waitcnt lgkmcnt(9)
	v_mfma_f32_16x16x32_bf16 v[64:67], v[176:179], v[104:107], v[64:67]
	v_cvt_pk_bf16_f32 v204, v84, v85
	v_mfma_f32_16x16x32_bf16 v[68:71], v[176:179], v[120:123], v[68:71]
	v_exp_f32_e32 v91, v91
	ds_read_b128 v[172:175], v209 offset:59392
	ds_write_b64 v228, v[150:151] offset:16384
	s_waitcnt lgkmcnt(10)
	v_mfma_f32_16x16x32_bf16 v[16:19], v[180:183], v[216:219], v[16:19]
	v_exp_f32_e32 v95, v95
	v_mfma_f32_16x16x32_bf16 v[20:23], v[180:183], v[238:241], v[20:23]
	v_cvt_pk_bf16_f32 v205, v86, v87
	v_add_f32_e32 v220, v220, v88
	ds_read_b128 v[176:179], v203 offset:4096
	ds_write_b64 v229, v[144:145] offset:16384
	s_waitcnt lgkmcnt(11)
	v_mfma_f32_16x16x32_bf16 v[68:71], v[230:233], v[124:127], v[68:71]
	v_add_f32_e32 v221, v221, v92
	v_add_f32_e32 v220, v220, v89
	v_mfma_f32_16x16x32_bf16 v[64:67], v[230:233], v[108:111], v[64:67]
	v_add_f32_e32 v221, v221, v93
	v_cvt_pk_bf16_f32 v244, v88, v89
	ds_read_b128 v[180:183], v209 offset:61440
	ds_write_b64 v184, v[146:147] offset:16384
	s_waitcnt lgkmcnt(12)
	v_mfma_f32_16x16x32_bf16 v[28:31], v[234:237], v[238:241], v[28:31]
	v_cvt_pk_bf16_f32 v245, v90, v91
	v_cvt_pk_bf16_f32 v206, v92, v93
	v_mfma_f32_16x16x32_bf16 v[24:27], v[234:237], v[216:219], v[24:27]
	v_cvt_pk_bf16_f32 v207, v94, v95
	ds_read_b128 v[230:233], v246 offset:4096
	global_load_dwordx4 v[148:151], v198, s[8:9]
	s_waitcnt lgkmcnt(12)
	v_mfma_f32_16x16x32_bf16 v[72:75], v[160:163], v[96:99], 0
	v_add_f32_e32 v220, v220, v90
	v_add_f32_e32 v221, v221, v94
	v_mfma_f32_16x16x32_bf16 v[76:79], v[160:163], v[112:115], 0
	v_add_f32_e32 v220, v220, v91
	v_add_f32_e32 v221, v221, v95
	ds_read_b128 v[234:237], v209 offset:63488
	global_load_dwordx4 v[144:147], v199, s[8:9]
	s_waitcnt lgkmcnt(11)
	v_mfma_f32_16x16x32_bf16 v[32:35], v[164:167], v[216:219], v[32:35]
	v_add_f32_e32 v194, v194, v220
	v_add_f32_e32 v195, v195, v221
	v_mfma_f32_16x16x32_bf16 v[36:39], v[164:167], v[238:241], v[36:39]
	v_exp_f32_e32 v64, v64
	ds_read_b128 v[160:163], v201 offset:8192
	global_load_dwordx4 v[136:139], v196, s[6:7]
	s_waitcnt lgkmcnt(10)
	v_mfma_f32_16x16x32_bf16 v[76:79], v[168:171], v[116:119], v[76:79]
	v_exp_f32_e32 v68, v68
	v_mfma_f32_16x16x32_bf16 v[72:75], v[168:171], v[100:103], v[72:75]
	v_exp_f32_e32 v65, v65
	ds_read_b128 v[164:167], v210 offset:49152
	global_load_dwordx4 v[140:143], v197, s[6:7]
	s_waitcnt lgkmcnt(9)
	v_mfma_f32_16x16x32_bf16 v[44:47], v[172:175], v[238:241], v[44:47]
	v_exp_f32_e32 v69, v69
	v_mfma_f32_16x16x32_bf16 v[40:43], v[172:175], v[216:219], v[40:43]
	v_exp_f32_e32 v66, v66
	ds_read_b128 v[168:171], v202 offset:8192
	s_waitcnt lgkmcnt(8)
	v_mfma_f32_16x16x32_bf16 v[72:75], v[176:179], v[104:107], v[72:75]
	v_exp_f32_e32 v70, v70
	v_mfma_f32_16x16x32_bf16 v[76:79], v[176:179], v[120:123], v[76:79]
	v_exp_f32_e32 v67, v67
	ds_read_b128 v[172:175], v210 offset:51200
	s_waitcnt lgkmcnt(7)
	v_mfma_f32_16x16x32_bf16 v[48:51], v[180:183], v[216:219], v[48:51]
	v_exp_f32_e32 v71, v71
	v_mfma_f32_16x16x32_bf16 v[52:55], v[180:183], v[238:241], v[52:55]
	v_add_f32_e32 v220, v64, v65
	ds_read_b128 v[176:179], v203 offset:8192
	s_waitcnt lgkmcnt(6)
	v_mfma_f32_16x16x32_bf16 v[76:79], v[230:233], v[124:127], v[76:79]
	v_add_f32_e32 v221, v68, v69
	v_mfma_f32_16x16x32_bf16 v[72:75], v[230:233], v[108:111], v[72:75]
	v_add_f32_e32 v220, v220, v66
	ds_read_b128 v[180:183], v210 offset:53248
	s_waitcnt lgkmcnt(6)
	v_mfma_f32_16x16x32_bf16 v[60:63], v[234:237], v[238:241], v[60:63]
	v_add_f32_e32 v221, v221, v70
	v_add_f32_e32 v220, v220, v67
	v_mfma_f32_16x16x32_bf16 v[56:59], v[234:237], v[216:219], v[56:59]
	v_add_f32_e32 v221, v221, v71
	ds_read_b128 v[230:233], v246 offset:8192
	s_cmp_eq_u32 s100, 1
	s_cbranch_scc1 .Lattn_pa3_16
	s_setprio 1
	s_branch .Lattn_pb3_16

.Lattn_pb3_16:
	s_waitcnt lgkmcnt(6)
	v_mfma_f32_16x16x32_bf16 v[80:83], v[160:163], v[96:99], 0
	v_exp_f32_e32 v72, v72
	v_mfma_f32_16x16x32_bf16 v[84:87], v[160:163], v[112:115], 0
	v_exp_f32_e32 v76, v76
	ds_read_b128 v[234:237], v210 offset:55296
	s_waitcnt lgkmcnt(6)
	v_mfma_f32_16x16x32_bf16 v[0:3], v[164:167], v[242:245], v[0:3]
	v_exp_f32_e32 v73, v73
	v_mfma_f32_16x16x32_bf16 v[4:7], v[164:167], v[204:207], v[4:7]
	v_exp_f32_e32 v77, v77
	ds_read_b128 v[160:163], v201 offset:12288
	s_waitcnt lgkmcnt(6)
	v_mfma_f32_16x16x32_bf16 v[84:87], v[168:171], v[116:119], v[84:87]
	v_exp_f32_e32 v74, v74
	v_mfma_f32_16x16x32_bf16 v[80:83], v[168:171], v[100:103], v[80:83]
	v_exp_f32_e32 v78, v78
	ds_read_b128 v[164:167], v210 offset:57344
	s_waitcnt lgkmcnt(6)
	v_mfma_f32_16x16x32_bf16 v[12:15], v[172:175], v[204:207], v[12:15]
	v_exp_f32_e32 v75, v75
	v_mfma_f32_16x16x32_bf16 v[8:11], v[172:175], v[242:245], v[8:11]
	v_exp_f32_e32 v79, v79
	ds_read_b128 v[168:171], v202 offset:12288
	s_waitcnt lgkmcnt(6)
	v_mfma_f32_16x16x32_bf16 v[80:83], v[176:179], v[104:107], v[80:83]
	v_add_f32_e32 v220, v220, v72
	v_add_f32_e32 v221, v221, v76
	v_mfma_f32_16x16x32_bf16 v[84:87], v[176:179], v[120:123], v[84:87]
	v_add_f32_e32 v220, v220, v73
	ds_read_b128 v[172:175], v210 offset:59392
	s_add_u32 s10, s10, 0x200
	s_addc_u32 s11, s11, 0
	s_add_u32 s12, s12, 0x40000
	s_addc_u32 s13, s13, 0
	s_add_i32 s4, s4, 4
	s_cmpk_lt_u32 s4, 0x104
	s_cselect_b64 s[6:7], -1, 0
	s_and_b64 s[6:7], s[0:1], s[6:7]
	s_and_b64 vcc, exec, s[6:7]
	s_waitcnt lgkmcnt(6)
	v_mfma_f32_16x16x32_bf16 v[16:19], v[180:183], v[242:245], v[16:19]
	v_add_f32_e32 v221, v221, v77
	v_add_f32_e32 v220, v220, v74
	v_mfma_f32_16x16x32_bf16 v[20:23], v[180:183], v[204:207], v[20:23]
	v_add_f32_e32 v221, v221, v78
	ds_read_b128 v[176:179], v203 offset:12288
	s_waitcnt lgkmcnt(6)
	v_mfma_f32_16x16x32_bf16 v[84:87], v[230:233], v[124:127], v[84:87]
	v_add_f32_e32 v220, v220, v75
	v_add_f32_e32 v221, v221, v79
	v_mfma_f32_16x16x32_bf16 v[80:83], v[230:233], v[108:111], v[80:83]
	v_cvt_pk_bf16_f32 v216, v64, v65
	ds_read_b128 v[180:183], v210 offset:61440
	s_waitcnt lgkmcnt(6)
	v_mfma_f32_16x16x32_bf16 v[28:31], v[234:237], v[204:207], v[28:31]
	v_cvt_pk_bf16_f32 v217, v66, v67
	v_cvt_pk_bf16_f32 v238, v68, v69
	v_mfma_f32_16x16x32_bf16 v[24:27], v[234:237], v[242:245], v[24:27]
	v_cvt_pk_bf16_f32 v239, v70, v71
	ds_read_b128 v[230:233], v246 offset:12288
	s_waitcnt lgkmcnt(6)
	v_mfma_f32_16x16x32_bf16 v[88:91], v[160:163], v[96:99], 0
	v_exp_f32_e32 v80, v80
	v_mfma_f32_16x16x32_bf16 v[92:95], v[160:163], v[112:115], 0
	v_exp_f32_e32 v84, v84
	ds_read_b128 v[234:237], v210 offset:63488
	s_waitcnt lgkmcnt(6)
	v_mfma_f32_16x16x32_bf16 v[32:35], v[164:167], v[242:245], v[32:35]
	v_exp_f32_e32 v81, v81
	v_mfma_f32_16x16x32_bf16 v[36:39], v[164:167], v[204:207], v[36:39]
	v_exp_f32_e32 v85, v85
	s_waitcnt lgkmcnt(5)
	v_mfma_f32_16x16x32_bf16 v[92:95], v[168:171], v[116:119], v[92:95]
	v_exp_f32_e32 v82, v82
	v_mfma_f32_16x16x32_bf16 v[88:91], v[168:171], v[100:103], v[88:91]
	v_exp_f32_e32 v86, v86
	s_waitcnt lgkmcnt(4)
	v_mfma_f32_16x16x32_bf16 v[44:47], v[172:175], v[204:207], v[44:47]
	v_exp_f32_e32 v83, v83
	v_mfma_f32_16x16x32_bf16 v[40:43], v[172:175], v[242:245], v[40:43]
	v_exp_f32_e32 v87, v87
	s_waitcnt lgkmcnt(3)
	v_mfma_f32_16x16x32_bf16 v[88:91], v[176:179], v[104:107], v[88:91]
	v_add_f32_e32 v220, v220, v80
	v_add_f32_e32 v221, v221, v84
	v_mfma_f32_16x16x32_bf16 v[92:95], v[176:179], v[120:123], v[92:95]
	v_add_f32_e32 v220, v220, v81
	s_waitcnt lgkmcnt(2)
	v_mfma_f32_16x16x32_bf16 v[48:51], v[180:183], v[242:245], v[48:51]
	v_add_f32_e32 v221, v221, v85
	v_add_f32_e32 v220, v220, v82
	v_mfma_f32_16x16x32_bf16 v[52:55], v[180:183], v[204:207], v[52:55]
	v_add_f32_e32 v221, v221, v86
	s_waitcnt lgkmcnt(1)
	v_mfma_f32_16x16x32_bf16 v[92:95], v[230:233], v[124:127], v[92:95]
	v_add_f32_e32 v220, v220, v83
	v_add_f32_e32 v221, v221, v87
	v_mfma_f32_16x16x32_bf16 v[88:91], v[230:233], v[108:111], v[88:91]
	v_cvt_pk_bf16_f32 v218, v72, v73
	s_waitcnt lgkmcnt(0)
	v_mfma_f32_16x16x32_bf16 v[60:63], v[234:237], v[204:207], v[60:63]
	v_cvt_pk_bf16_f32 v219, v74, v75
	v_cvt_pk_bf16_f32 v240, v76, v77
	v_mfma_f32_16x16x32_bf16 v[56:59], v[234:237], v[242:245], v[56:59]
	v_cvt_pk_bf16_f32 v241, v78, v79
	s_cbranch_vccnz .LBB0_734
	s_setprio 0
	s_waitcnt vmcnt(0)
	s_nop 7
	s_nop 7
	ds_swizzle_b32 v64, v194 offset:swizzle(SWAP,16)
	s_waitcnt lgkmcnt(0)
	v_add_f32_e32 v194, v194, v64
	v_mov_b32_e32 v65, v194
	s_nop 1
	v_permlane32_swap_b32_e32 v194, v65
	v_add_f32_e32 v194, v194, v65
	s_nop 0
	v_rcp_f32_e32 v66, v194
	ds_swizzle_b32 v64, v195 offset:swizzle(SWAP,16)
	s_waitcnt lgkmcnt(0)
	v_add_f32_e32 v195, v195, v64
	v_mov_b32_e32 v65, v195
	s_nop 1
	v_permlane32_swap_b32_e32 v195, v65
	v_add_f32_e32 v195, v195, v65
	s_nop 0
	v_rcp_f32_e32 v67, v195
	v_readlane_b32 s100, v250, 8
	v_mbcnt_lo_u32_b32 v68, -1, 0
	v_mbcnt_hi_u32_b32 v68, -1, v68
	v_and_b32_e32 v69, 15, v68
	v_lshrrev_b32_e32 v70, 4, v68
	s_lshr_b32 s101, s100, 1
	v_add_u32_e32 v69, s101, v69
	v_lshlrev_b32_e32 v69, 12, v69
	v_and_b32_e32 v71, 1, v70
	v_lshlrev_b32_e32 v71, 5, v71
	v_and_b32_e32 v70, 2, v70
	v_lshl_add_u32 v71, v70, 3, v71
	v_add_u32_e32 v70, v69, v71
	v_add_u32_e32 v71, 0x10000, v70
	v_mul_f32_e32 v0, v0, v66
	v_mul_f32_e32 v1, v1, v66
	v_mul_f32_e32 v2, v2, v66
	v_mul_f32_e32 v3, v3, v66
	v_mul_f32_e32 v8, v8, v66
	v_mul_f32_e32 v9, v9, v66
	v_mul_f32_e32 v10, v10, v66
	v_mul_f32_e32 v11, v11, v66
	v_cvt_pk_bf16_f32 v72, v0, v1
	v_cvt_pk_bf16_f32 v73, v2, v3
	v_cvt_pk_bf16_f32 v74, v8, v9
	v_cvt_pk_bf16_f32 v75, v10, v11
	s_nop 1
	v_permlane16_swap_b32_e32 v72, v74
	v_permlane16_swap_b32_e32 v73, v75
	s_nop 1
	global_store_dwordx4 v70, v[72:75], s[58:59] offset:0
	v_mul_f32_e32 v16, v16, v66
	v_mul_f32_e32 v17, v17, v66
	v_mul_f32_e32 v18, v18, v66
	v_mul_f32_e32 v19, v19, v66
	v_mul_f32_e32 v24, v24, v66
	v_mul_f32_e32 v25, v25, v66
	v_mul_f32_e32 v26, v26, v66
	v_mul_f32_e32 v27, v27, v66
	v_cvt_pk_bf16_f32 v76, v16, v17
	v_cvt_pk_bf16_f32 v77, v18, v19
	v_cvt_pk_bf16_f32 v78, v24, v25
	v_cvt_pk_bf16_f32 v79, v26, v27
	s_nop 1
	v_permlane16_swap_b32_e32 v76, v78
	v_permlane16_swap_b32_e32 v77, v79
	s_nop 1
	global_store_dwordx4 v70, v[76:79], s[58:59] offset:64
	v_mul_f32_e32 v32, v32, v66
	v_mul_f32_e32 v33, v33, v66
	v_mul_f32_e32 v34, v34, v66
	v_mul_f32_e32 v35, v35, v66
	v_mul_f32_e32 v40, v40, v66
	v_mul_f32_e32 v41, v41, v66
	v_mul_f32_e32 v42, v42, v66
	v_mul_f32_e32 v43, v43, v66
	v_cvt_pk_bf16_f32 v80, v32, v33
	v_cvt_pk_bf16_f32 v81, v34, v35
	v_cvt_pk_bf16_f32 v82, v40, v41
	v_cvt_pk_bf16_f32 v83, v42, v43
	s_nop 1
	v_permlane16_swap_b32_e32 v80, v82
	v_permlane16_swap_b32_e32 v81, v83
	s_nop 1
	global_store_dwordx4 v70, v[80:83], s[58:59] offset:128
	v_mul_f32_e32 v48, v48, v66
	v_mul_f32_e32 v49, v49, v66
	v_mul_f32_e32 v50, v50, v66
	v_mul_f32_e32 v51, v51, v66
	v_mul_f32_e32 v56, v56, v66
	v_mul_f32_e32 v57, v57, v66
	v_mul_f32_e32 v58, v58, v66
	v_mul_f32_e32 v59, v59, v66
	v_cvt_pk_bf16_f32 v84, v48, v49
	v_cvt_pk_bf16_f32 v85, v50, v51
	v_cvt_pk_bf16_f32 v86, v56, v57
	v_cvt_pk_bf16_f32 v87, v58, v59
	s_nop 1
	v_permlane16_swap_b32_e32 v84, v86
	v_permlane16_swap_b32_e32 v85, v87
	s_nop 1
	global_store_dwordx4 v70, v[84:87], s[58:59] offset:192
	v_mul_f32_e32 v4, v4, v67
	v_mul_f32_e32 v5, v5, v67
	v_mul_f32_e32 v6, v6, v67
	v_mul_f32_e32 v7, v7, v67
	v_mul_f32_e32 v12, v12, v67
	v_mul_f32_e32 v13, v13, v67
	v_mul_f32_e32 v14, v14, v67
	v_mul_f32_e32 v15, v15, v67
	v_cvt_pk_bf16_f32 v88, v4, v5
	v_cvt_pk_bf16_f32 v89, v6, v7
	v_cvt_pk_bf16_f32 v90, v12, v13
	v_cvt_pk_bf16_f32 v91, v14, v15
	s_nop 1
	v_permlane16_swap_b32_e32 v88, v90
	v_permlane16_swap_b32_e32 v89, v91
	s_nop 1
	global_store_dwordx4 v71, v[88:91], s[58:59] offset:0
	v_mul_f32_e32 v20, v20, v67
	v_mul_f32_e32 v21, v21, v67
	v_mul_f32_e32 v22, v22, v67
	v_mul_f32_e32 v23, v23, v67
	v_mul_f32_e32 v28, v28, v67
	v_mul_f32_e32 v29, v29, v67
	v_mul_f32_e32 v30, v30, v67
	v_mul_f32_e32 v31, v31, v67
	v_cvt_pk_bf16_f32 v92, v20, v21
	v_cvt_pk_bf16_f32 v93, v22, v23
	v_cvt_pk_bf16_f32 v94, v28, v29
	v_cvt_pk_bf16_f32 v95, v30, v31
	s_nop 1
	v_permlane16_swap_b32_e32 v92, v94
	v_permlane16_swap_b32_e32 v93, v95
	s_nop 1
	global_store_dwordx4 v71, v[92:95], s[58:59] offset:64
	v_mul_f32_e32 v36, v36, v67
	v_mul_f32_e32 v37, v37, v67
	v_mul_f32_e32 v38, v38, v67
	v_mul_f32_e32 v39, v39, v67
	v_mul_f32_e32 v44, v44, v67
	v_mul_f32_e32 v45, v45, v67
	v_mul_f32_e32 v46, v46, v67
	v_mul_f32_e32 v47, v47, v67
	v_cvt_pk_bf16_f32 v72, v36, v37
	v_cvt_pk_bf16_f32 v73, v38, v39
	v_cvt_pk_bf16_f32 v74, v44, v45
	v_cvt_pk_bf16_f32 v75, v46, v47
	s_nop 1
	v_permlane16_swap_b32_e32 v72, v74
	v_permlane16_swap_b32_e32 v73, v75
	s_nop 1
	global_store_dwordx4 v71, v[72:75], s[58:59] offset:128
	v_mul_f32_e32 v52, v52, v67
	v_mul_f32_e32 v53, v53, v67
	v_mul_f32_e32 v54, v54, v67
	v_mul_f32_e32 v55, v55, v67
	v_mul_f32_e32 v60, v60, v67
	v_mul_f32_e32 v61, v61, v67
	v_mul_f32_e32 v62, v62, v67
	v_mul_f32_e32 v63, v63, v67
	v_cvt_pk_bf16_f32 v76, v52, v53
	v_cvt_pk_bf16_f32 v77, v54, v55
	v_cvt_pk_bf16_f32 v78, v60, v61
	v_cvt_pk_bf16_f32 v79, v62, v63
	s_nop 1
	v_permlane16_swap_b32_e32 v76, v78
	v_permlane16_swap_b32_e32 v77, v79
	s_nop 1
	global_store_dwordx4 v71, v[76:79], s[58:59] offset:192
	s_barrier
